# cross-attention epilogue: 32 two-byte write-through stores per lane replaced by an LDS transpose (dead K/V area) and 4 write-through dwordx4 stores of 1 KiB
# baseline (speedup 1.0000x reference)
.LBB0_1273:
	v_cvt_pk_bf16_f32 v60, v64, v65
	v_cvt_pk_bf16_f32 v61, v66, v67
	v_cvt_pk_bf16_f32 v62, v68, v69
	v_cvt_pk_bf16_f32 v63, v70, v71
	ds_read_b64_tr_b16 v[64:65], v91 offset:30720
	ds_read_b64_tr_b16 v[66:67], v91 offset:32256
	s_waitcnt lgkmcnt(0)
	v_mfma_f32_32x32x16_bf16 v[0:15], v[60:63], v[64:67], v[0:15]
	ds_read_b64_tr_b16 v[66:67], v91 offset:32320
	ds_read_b64_tr_b16 v[64:65], v91 offset:30784
	v_cvt_pk_bf16_f32 v52, v51, v52
	v_cvt_pk_bf16_f32 v53, v53, v54
	v_cvt_pk_bf16_f32 v54, v55, v56
	v_cvt_pk_bf16_f32 v55, v57, v58
	ds_read_b64_tr_b16 v[56:57], v91 offset:33792
	ds_read_b64_tr_b16 v[58:59], v91 offset:35328
	v_cvt_pk_bf16_f32 v32, v32, v33
	s_waitcnt lgkmcnt(2)
	v_mfma_f32_32x32x16_bf16 v[16:31], v[60:63], v[64:67], v[16:31]
	v_cvt_pk_bf16_f32 v33, v34, v35
	v_cvt_pk_bf16_f32 v34, v36, v48
	v_cvt_pk_bf16_f32 v35, v38, v49
	v_cvt_pk_bf16_f32 v36, v37, v39
	v_cvt_pk_bf16_f32 v37, v41, v50
	v_cvt_pk_bf16_f32 v38, v44, v45
	v_cvt_pk_bf16_f32 v39, v46, v47
	s_waitcnt lgkmcnt(0)
	v_mfma_f32_32x32x16_bf16 v[0:15], v[52:55], v[56:59], v[0:15]
	ds_read_b64_tr_b16 v[58:59], v91 offset:35392
	ds_read_b64_tr_b16 v[56:57], v91 offset:33856
	s_lshl_b64 s[4:5], s[4:5], 1
	s_add_u32 s4, s12, s4
	s_addc_u32 s5, s13, s5
	s_lshl_b32 s6, s23, 1
	s_add_u32 s4, s4, s6
	s_addc_u32 s5, s5, 0
	s_waitcnt lgkmcnt(0)
	v_mfma_f32_32x32x16_bf16 v[16:31], v[52:55], v[56:59], v[16:31]
	ds_read_b64_tr_b16 v[52:53], v91 offset:36864
	ds_read_b64_tr_b16 v[54:55], v91 offset:38400
	s_waitcnt lgkmcnt(0)
	v_mfma_f32_32x32x16_bf16 v[0:15], v[32:35], v[52:55], v[0:15]
	ds_read_b64_tr_b16 v[54:55], v91 offset:38464
	ds_read_b64_tr_b16 v[52:53], v91 offset:36928
	s_waitcnt lgkmcnt(0)
	v_mfma_f32_32x32x16_bf16 v[16:31], v[32:35], v[52:55], v[16:31]
	ds_read_b64_tr_b16 v[32:33], v91 offset:39936
	ds_read_b64_tr_b16 v[34:35], v91 offset:41472
	ds_read_b64_tr_b16 v[46:47], v91 offset:41536
	ds_read_b64_tr_b16 v[44:45], v91 offset:40000
	s_waitcnt lgkmcnt(2)
	v_mfma_f32_32x32x16_bf16 v[0:15], v[36:39], v[32:35], v[0:15]
	s_waitcnt lgkmcnt(0)
	v_mfma_f32_32x32x16_bf16 v[16:31], v[36:39], v[44:47], v[16:31]
	v_add_f32_e32 v32, v42, v43
	v_fmac_f32_e32 v32, v99, v40
	v_div_scale_f32 v33, s[6:7], v32, v32, 1.0
	v_rcp_f32_e32 v34, v33
	s_barrier
	v_fma_f32 v35, -v33, v34, 1.0
	v_fmac_f32_e32 v34, v35, v34
	v_div_scale_f32 v35, vcc, 1.0, v32, 1.0
	v_mul_f32_e32 v36, v35, v34
	v_fma_f32 v37, -v33, v36, v35
	v_fmac_f32_e32 v36, v37, v34
	v_fma_f32 v33, -v33, v36, v35
	v_div_fmas_f32 v33, v33, v34, v36
	v_div_fixup_f32 v32, v33, v32, 1.0
	v_ashrrev_i32_e32 v48, 5, v96
	v_lshl_add_u32 v33, v96, 2, s25
	ds_write_b32 v33, v32 offset:43008
	v_lshl_add_u32 v44, v48, 4, s25
	ds_read_b128 v[32:35], v44 offset:43008
	ds_read_b128 v[36:39], v44 offset:43040
	ds_read_b128 v[40:43], v44 offset:43072
	ds_read_b128 v[44:47], v44 offset:43104
	s_waitcnt lgkmcnt(0)
	v_mul_f32_e32 v0, v0, v32
	v_mul_f32_e32 v1, v1, v33
	v_mul_f32_e32 v2, v2, v34
	v_mul_f32_e32 v3, v3, v35
	v_mul_f32_e32 v4, v4, v36
	v_mul_f32_e32 v5, v5, v37
	v_mul_f32_e32 v6, v6, v38
	v_mul_f32_e32 v7, v7, v39
	v_mul_f32_e32 v8, v8, v40
	v_mul_f32_e32 v9, v9, v41
	v_mul_f32_e32 v10, v10, v42
	v_mul_f32_e32 v11, v11, v43
	v_mul_f32_e32 v12, v12, v44
	v_mul_f32_e32 v13, v13, v45
	v_mul_f32_e32 v14, v14, v46
	v_mul_f32_e32 v15, v15, v47
	v_mul_f32_e32 v16, v16, v32
	v_mul_f32_e32 v17, v17, v33
	v_mul_f32_e32 v18, v18, v34
	v_mul_f32_e32 v19, v19, v35
	v_mul_f32_e32 v20, v20, v36
	v_mul_f32_e32 v21, v21, v37
	v_mul_f32_e32 v22, v22, v38
	v_mul_f32_e32 v23, v23, v39
	v_mul_f32_e32 v24, v24, v40
	v_mul_f32_e32 v25, v25, v41
	v_mul_f32_e32 v26, v26, v42
	v_mul_f32_e32 v27, v27, v43
	v_mul_f32_e32 v28, v28, v44
	v_mul_f32_e32 v29, v29, v45
	v_mul_f32_e32 v30, v30, v46
	v_mul_f32_e32 v31, v31, v47
	v_bfe_u32 v32, v0, 16, 1
	v_add3_u32 v0, v0, v32, s63
	v_bfe_u32 v33, v1, 16, 1
	v_add3_u32 v1, v1, v33, s63
	v_bfe_u32 v34, v2, 16, 1
	v_add3_u32 v2, v2, v34, s63
	v_bfe_u32 v35, v3, 16, 1
	v_add3_u32 v3, v3, v35, s63
	v_bfe_u32 v36, v4, 16, 1
	v_add3_u32 v4, v4, v36, s63
	v_bfe_u32 v37, v5, 16, 1
	v_add3_u32 v5, v5, v37, s63
	v_bfe_u32 v38, v6, 16, 1
	v_add3_u32 v6, v6, v38, s63
	v_bfe_u32 v39, v7, 16, 1
	v_add3_u32 v7, v7, v39, s63
	v_bfe_u32 v40, v8, 16, 1
	v_add3_u32 v8, v8, v40, s63
	v_bfe_u32 v41, v9, 16, 1
	v_add3_u32 v9, v9, v41, s63
	v_bfe_u32 v42, v10, 16, 1
	v_add3_u32 v10, v10, v42, s63
	v_bfe_u32 v43, v11, 16, 1
	v_add3_u32 v11, v11, v43, s63
	v_bfe_u32 v44, v12, 16, 1
	v_add3_u32 v12, v12, v44, s63
	v_bfe_u32 v45, v13, 16, 1
	v_add3_u32 v13, v13, v45, s63
	v_bfe_u32 v46, v14, 16, 1
	v_add3_u32 v14, v14, v46, s63
	v_bfe_u32 v47, v15, 16, 1
	v_add3_u32 v15, v15, v47, s63
	v_bfe_u32 v32, v16, 16, 1
	v_add3_u32 v16, v16, v32, s63
	v_bfe_u32 v33, v17, 16, 1
	v_add3_u32 v17, v17, v33, s63
	v_bfe_u32 v34, v18, 16, 1
	v_add3_u32 v18, v18, v34, s63
	v_bfe_u32 v35, v19, 16, 1
	v_add3_u32 v19, v19, v35, s63
	v_bfe_u32 v36, v20, 16, 1
	v_add3_u32 v20, v20, v36, s63
	v_bfe_u32 v37, v21, 16, 1
	v_add3_u32 v21, v21, v37, s63
	v_bfe_u32 v38, v22, 16, 1
	v_add3_u32 v22, v22, v38, s63
	v_bfe_u32 v39, v23, 16, 1
	v_add3_u32 v23, v23, v39, s63
	v_bfe_u32 v40, v24, 16, 1
	v_add3_u32 v24, v24, v40, s63
	v_bfe_u32 v41, v25, 16, 1
	v_add3_u32 v25, v25, v41, s63
	v_bfe_u32 v42, v26, 16, 1
	v_add3_u32 v26, v26, v42, s63
	v_bfe_u32 v43, v27, 16, 1
	v_add3_u32 v27, v27, v43, s63
	v_bfe_u32 v44, v28, 16, 1
	v_add3_u32 v28, v28, v44, s63
	v_bfe_u32 v45, v29, 16, 1
	v_add3_u32 v29, v29, v45, s63
	v_bfe_u32 v46, v30, 16, 1
	v_add3_u32 v30, v30, v46, s63
	v_bfe_u32 v47, v31, 16, 1
	v_add3_u32 v31, v31, v47, s63
	s_lshl_b32 s6, s25, 4
	v_and_b32_e32 v49, 31, v96
	v_lshlrev_b32_e32 v49, 1, v49
	v_lshl_add_u32 v49, v48, 9, v49
	v_add_u32_e32 v49, s6, v49
	ds_write_b16_d16_hi v49, v0 offset:0
	ds_write_b16_d16_hi v49, v16 offset:64
	ds_write_b16_d16_hi v49, v1 offset:128
	ds_write_b16_d16_hi v49, v17 offset:192
	ds_write_b16_d16_hi v49, v2 offset:256
	ds_write_b16_d16_hi v49, v18 offset:320
	ds_write_b16_d16_hi v49, v3 offset:384
	ds_write_b16_d16_hi v49, v19 offset:448
	ds_write_b16_d16_hi v49, v4 offset:1024
	ds_write_b16_d16_hi v49, v20 offset:1088
	ds_write_b16_d16_hi v49, v5 offset:1152
	ds_write_b16_d16_hi v49, v21 offset:1216
	ds_write_b16_d16_hi v49, v6 offset:1280
	ds_write_b16_d16_hi v49, v22 offset:1344
	ds_write_b16_d16_hi v49, v7 offset:1408
	ds_write_b16_d16_hi v49, v23 offset:1472
	ds_write_b16_d16_hi v49, v8 offset:2048
	ds_write_b16_d16_hi v49, v24 offset:2112
	ds_write_b16_d16_hi v49, v9 offset:2176
	ds_write_b16_d16_hi v49, v25 offset:2240
	ds_write_b16_d16_hi v49, v10 offset:2304
	ds_write_b16_d16_hi v49, v26 offset:2368
	ds_write_b16_d16_hi v49, v11 offset:2432
	ds_write_b16_d16_hi v49, v27 offset:2496
	ds_write_b16_d16_hi v49, v12 offset:3072
	ds_write_b16_d16_hi v49, v28 offset:3136
	ds_write_b16_d16_hi v49, v13 offset:3200
	ds_write_b16_d16_hi v49, v29 offset:3264
	ds_write_b16_d16_hi v49, v14 offset:3328
	ds_write_b16_d16_hi v49, v30 offset:3392
	ds_write_b16_d16_hi v49, v15 offset:3456
	ds_write_b16_d16_hi v49, v31 offset:3520
	v_lshrrev_b32_e32 v50, 3, v96
	v_and_b32_e32 v51, 7, v96
	v_lshlrev_b32_e32 v208, 4, v51
	v_lshl_add_u32 v52, v50, 7, v208
	v_add_u32_e32 v52, s6, v52
	v_add_u32_e32 v54, s24, v50
	v_ashrrev_i32_e32 v55, 31, v54
	v_lshlrev_b64 v[54:55], 9, v[54:55]
	v_lshl_add_u64 v[56:57], s[4:5], 0, v[208:209]
	v_lshl_add_u64 v[56:57], v[56:57], 0, v[54:55]
	s_movk_i32 s6, 0x1000
	s_mov_b32 s7, 0
	ds_read_b128 v[32:35], v52
	ds_read_b128 v[36:39], v52 offset:1024
	ds_read_b128 v[40:43], v52 offset:2048
	ds_read_b128 v[44:47], v52 offset:3072
	s_waitcnt lgkmcnt(3)
	global_store_dwordx4 v[56:57], v[32:35], off sc1
	v_lshl_add_u64 v[56:57], v[56:57], 0, s[6:7]
	s_waitcnt lgkmcnt(2)
	global_store_dwordx4 v[56:57], v[36:39], off sc1
	v_lshl_add_u64 v[56:57], v[56:57], 0, s[6:7]
	s_waitcnt lgkmcnt(1)
	global_store_dwordx4 v[56:57], v[40:43], off sc1
	v_lshl_add_u64 v[56:57], v[56:57], 0, s[6:7]
	s_waitcnt lgkmcnt(0)
	global_store_dwordx4 v[56:57], v[44:47], off sc1
	s_barrier
	s_waitcnt vmcnt(0)
	s_and_saveexec_b64 s[4:5], s[0:1]
	s_cbranch_execz .LBB0_1265
	s_mov_b64 s[6:7], exec
	v_mbcnt_lo_u32_b32 v0, s6, 0
	v_mbcnt_hi_u32_b32 v0, s7, v0
	v_cmp_eq_u32_e32 vcc, 0, v0
	s_and_b64 s[24:25], exec, vcc
	s_mov_b64 exec, s[24:25]
	s_cbranch_execz .LBB0_1265
	s_lshl_b32 s22, s22, 4
	s_lshl_b32 s21, s21, 7
	s_or_b32 s22, s22, s18
	s_add_i32 s22, s21, s22
	s_ashr_i32 s23, s22, 31
	s_lshl_b64 s[22:23], s[22:23], 2
	s_add_u32 s22, s16, s22
	s_addc_u32 s23, s17, s23
	s_bcnt1_i32_b64 s6, s[6:7]
	v_mov_b32_e32 v0, s6
	global_atomic_add v209, v0, s[22:23]
	s_branch .LBB0_1265
